# speedup vs baseline: 1.0155x; 1.0019x over previous
.LBB5_23:
	s_add_i32 s1, s10, s6
	s_add_i32 s7, s1, -4
	s_min_u32 s1, s7, s1
	s_mul_i32 s7, s1, 0x180
	v_add_u32_e32 v33, s7, v32
	ds_read_b128 v[108:111], v33
	ds_read_b128 v[112:115], v33 offset:64
	ds_read_b128 v[116:119], v33 offset:24832
	ds_read_b128 v[120:123], v33 offset:24896
	ds_read_b128 v[154:157], v33 offset:128
	ds_read_b128 v[158:161], v33 offset:192
	ds_read_b128 v[162:165], v33 offset:24960
	ds_read_b128 v[166:169], v33 offset:25024
	ds_read_b128 v[174:177], v33 offset:256
	ds_read_b128 v[178:181], v33 offset:320
	ds_read_b128 v[182:185], v33 offset:25088
	ds_read_b128 v[186:189], v33 offset:25152
	s_mul_i32 s7, s1, 0xc00
	s_addk_i32 s7, 0xc00
	s_cmp_lt_i32 s1, 3
	s_cselect_b32 s8, s7, 0
	s_ashr_i32 s9, s8, 31
	s_setprio 1
	s_waitcnt vmcnt(17) lgkmcnt(11)
	v_mfma_f32_16x16x32_bf16 v[22:25], v[108:111], v[92:95], v[22:25]
	s_waitcnt lgkmcnt(9)
	v_mfma_f32_16x16x32_bf16 v[18:21], v[116:119], v[92:95], v[18:21]
	s_waitcnt vmcnt(13)
	v_mfma_f32_16x16x32_bf16 v[14:17], v[108:111], v[104:107], v[14:17]
	v_mfma_f32_16x16x32_bf16 v[10:13], v[116:119], v[104:107], v[10:13]
	s_waitcnt vmcnt(11)
	v_mfma_f32_16x16x32_bf16 v[6:9], v[108:111], v[100:103], v[6:9]
	v_mfma_f32_16x16x32_bf16 v[2:5], v[116:119], v[100:103], v[2:5]
	s_setprio 0
	s_lshl_b64 s[8:9], s[8:9], 1
	v_lshl_add_u64 v[34:35], v[26:27], 0, s[8:9]
	v_lshl_add_u64 v[110:111], v[30:31], 0, s[8:9]
	v_lshl_add_u64 v[108:109], v[28:29], 0, s[8:9]
	global_load_dwordx4 v[92:95], v[34:35], off
	global_load_dwordx4 v[104:107], v[108:109], off
	global_load_dwordx4 v[100:103], v[110:111], off
	s_setprio 1
	v_mfma_f32_16x16x32_bf16 v[22:25], v[112:115], v[72:75], v[22:25]
	s_waitcnt lgkmcnt(8)
	v_mfma_f32_16x16x32_bf16 v[18:21], v[120:123], v[72:75], v[18:21]
	v_mfma_f32_16x16x32_bf16 v[14:17], v[112:115], v[84:87], v[14:17]
	v_mfma_f32_16x16x32_bf16 v[10:13], v[120:123], v[84:87], v[10:13]
	s_waitcnt vmcnt(13)
	v_mfma_f32_16x16x32_bf16 v[6:9], v[112:115], v[76:79], v[6:9]
	v_mfma_f32_16x16x32_bf16 v[2:5], v[120:123], v[76:79], v[2:5]
	s_setprio 0
	global_load_dwordx4 v[72:75], v[34:35], off offset:1024
	global_load_dwordx4 v[84:87], v[108:109], off offset:1024
	global_load_dwordx4 v[76:79], v[110:111], off offset:1024
	s_setprio 1
	s_waitcnt lgkmcnt(7)
	v_mfma_f32_16x16x32_bf16 v[22:25], v[154:157], v[52:55], v[22:25]
	s_waitcnt lgkmcnt(5)
	v_mfma_f32_16x16x32_bf16 v[18:21], v[162:165], v[52:55], v[18:21]
	s_waitcnt vmcnt(15)
	v_mfma_f32_16x16x32_bf16 v[14:17], v[154:157], v[60:63], v[14:17]
	v_mfma_f32_16x16x32_bf16 v[10:13], v[162:165], v[60:63], v[10:13]
	s_waitcnt vmcnt(13)
	v_mfma_f32_16x16x32_bf16 v[6:9], v[154:157], v[56:59], v[6:9]
	v_mfma_f32_16x16x32_bf16 v[2:5], v[162:165], v[56:59], v[2:5]
	s_setprio 0
	global_load_dwordx4 v[52:55], v[34:35], off offset:2048
	global_load_dwordx4 v[60:63], v[108:109], off offset:2048
	global_load_dwordx4 v[56:59], v[110:111], off offset:2048
	s_setprio 1
	v_mfma_f32_16x16x32_bf16 v[22:25], v[158:161], v[36:39], v[22:25]
	s_waitcnt lgkmcnt(4)
	v_mfma_f32_16x16x32_bf16 v[18:21], v[166:169], v[36:39], v[18:21]
	v_mfma_f32_16x16x32_bf16 v[14:17], v[158:161], v[48:51], v[14:17]
	v_mfma_f32_16x16x32_bf16 v[10:13], v[166:169], v[48:51], v[10:13]
	s_waitcnt vmcnt(15)
	v_mfma_f32_16x16x32_bf16 v[6:9], v[158:161], v[44:47], v[6:9]
	v_mfma_f32_16x16x32_bf16 v[2:5], v[166:169], v[44:47], v[2:5]
	s_setprio 0
	global_load_dwordx4 v[36:39], v[34:35], off offset:3072
	global_load_dwordx4 v[48:51], v[108:109], off offset:3072
	global_load_dwordx4 v[44:47], v[110:111], off offset:3072
	s_setprio 1
	s_waitcnt vmcnt(15) lgkmcnt(3)
	v_mfma_f32_16x16x32_bf16 v[22:25], v[174:177], v[80:83], v[22:25]
	s_waitcnt lgkmcnt(1)
	v_mfma_f32_16x16x32_bf16 v[18:21], v[182:185], v[80:83], v[18:21]
	v_mfma_f32_16x16x32_bf16 v[14:17], v[174:177], v[64:67], v[14:17]
	v_mfma_f32_16x16x32_bf16 v[10:13], v[182:185], v[64:67], v[10:13]
	v_mfma_f32_16x16x32_bf16 v[6:9], v[174:177], v[68:71], v[6:9]
	v_mfma_f32_16x16x32_bf16 v[2:5], v[182:185], v[68:71], v[2:5]
	s_setprio 0
	v_add_co_u32_e32 v34, vcc, s0, v34
	s_nop 1
	v_addc_co_u32_e32 v35, vcc, 0, v35, vcc
	v_add_co_u32_e32 v108, vcc, s0, v108
	s_nop 1
	v_addc_co_u32_e32 v109, vcc, 0, v109, vcc
	v_add_co_u32_e32 v110, vcc, s0, v110
	global_load_dwordx4 v[80:83], v[34:35], off
	global_load_dwordx4 v[64:67], v[108:109], off
	v_addc_co_u32_e32 v111, vcc, 0, v111, vcc
	global_load_dwordx4 v[68:71], v[110:111], off
	s_setprio 1
	s_waitcnt vmcnt(17)
	v_mfma_f32_16x16x32_bf16 v[22:25], v[178:181], v[40:43], v[22:25]
	s_waitcnt lgkmcnt(0)
	v_mfma_f32_16x16x32_bf16 v[18:21], v[186:189], v[40:43], v[18:21]
	s_waitcnt vmcnt(16)
	v_mfma_f32_16x16x32_bf16 v[14:17], v[178:181], v[96:99], v[14:17]
	v_mfma_f32_16x16x32_bf16 v[10:13], v[186:189], v[96:99], v[10:13]
	s_waitcnt vmcnt(15)
	v_mfma_f32_16x16x32_bf16 v[6:9], v[178:181], v[88:91], v[6:9]
	v_mfma_f32_16x16x32_bf16 v[2:5], v[186:189], v[88:91], v[2:5]
	s_setprio 0
	global_load_dwordx4 v[40:43], v[34:35], off offset:1024
	global_load_dwordx4 v[96:99], v[108:109], off offset:1024
	global_load_dwordx4 v[88:91], v[110:111], off offset:1024
	s_add_i32 s6, s6, 1
	s_cmp_lg_u32 s6, 3
	s_cbranch_scc1 .LBB5_23
	s_mul_i32 s0, s10, 0xc0
	s_add_i32 s6, s0, 0xffffff40
	s_and_b64 s[0:1], s[2:3], exec
	s_cselect_b32 s0, 0x240, s6
	v_lshl_add_u32 v34, s0, 1, v32
	ds_read_b128 v[26:29], v34
	ds_read_b128 v[30:33], v34 offset:64
	ds_read_b128 v[108:111], v34 offset:24832
	ds_read_b128 v[112:115], v34 offset:24896
	ds_read_b128 v[116:119], v34 offset:128
	ds_read_b128 v[120:123], v34 offset:192
	ds_read_b128 v[154:157], v34 offset:24960
	ds_read_b128 v[158:161], v34 offset:25024
	ds_read_b128 v[162:165], v34 offset:256
	ds_read_b128 v[166:169], v34 offset:320
	ds_read_b128 v[174:177], v34 offset:25088
	ds_read_b128 v[178:181], v34 offset:25152
	s_setprio 1
	s_waitcnt vmcnt(17) lgkmcnt(11)
	v_mfma_f32_16x16x32_bf16 v[22:25], v[26:29], v[92:95], v[22:25]
	s_waitcnt lgkmcnt(9)
	v_mfma_f32_16x16x32_bf16 v[18:21], v[108:111], v[92:95], v[18:21]
	s_waitcnt vmcnt(16)
	v_mfma_f32_16x16x32_bf16 v[14:17], v[26:29], v[104:107], v[14:17]
	v_mfma_f32_16x16x32_bf16 v[10:13], v[108:111], v[104:107], v[10:13]
	s_waitcnt vmcnt(15)
	v_mfma_f32_16x16x32_bf16 v[6:9], v[26:29], v[100:103], v[6:9]
	v_mfma_f32_16x16x32_bf16 v[2:5], v[108:111], v[100:103], v[2:5]
	s_setprio 0
	s_setprio 1
	s_waitcnt vmcnt(14)
	v_mfma_f32_16x16x32_bf16 v[22:25], v[30:33], v[72:75], v[22:25]
	s_waitcnt lgkmcnt(8)
	v_mfma_f32_16x16x32_bf16 v[18:21], v[112:115], v[72:75], v[18:21]
	s_waitcnt vmcnt(13)
	v_mfma_f32_16x16x32_bf16 v[14:17], v[30:33], v[84:87], v[14:17]
	v_mfma_f32_16x16x32_bf16 v[10:13], v[112:115], v[84:87], v[10:13]
	s_waitcnt vmcnt(12)
	v_mfma_f32_16x16x32_bf16 v[6:9], v[30:33], v[76:79], v[6:9]
	v_mfma_f32_16x16x32_bf16 v[2:5], v[112:115], v[76:79], v[2:5]
	s_setprio 0
	s_setprio 1
	s_waitcnt vmcnt(11) lgkmcnt(7)
	v_mfma_f32_16x16x32_bf16 v[22:25], v[116:119], v[52:55], v[22:25]
	s_waitcnt lgkmcnt(5)
	v_mfma_f32_16x16x32_bf16 v[18:21], v[154:157], v[52:55], v[18:21]
	s_waitcnt vmcnt(10)
	v_mfma_f32_16x16x32_bf16 v[14:17], v[116:119], v[60:63], v[14:17]
	v_mfma_f32_16x16x32_bf16 v[10:13], v[154:157], v[60:63], v[10:13]
	s_waitcnt vmcnt(9)
	v_mfma_f32_16x16x32_bf16 v[6:9], v[116:119], v[56:59], v[6:9]
	v_mfma_f32_16x16x32_bf16 v[2:5], v[154:157], v[56:59], v[2:5]
	s_setprio 0
	s_setprio 1
	s_waitcnt vmcnt(8)
	v_mfma_f32_16x16x32_bf16 v[22:25], v[120:123], v[36:39], v[22:25]
	s_waitcnt lgkmcnt(4)
	v_mfma_f32_16x16x32_bf16 v[18:21], v[158:161], v[36:39], v[18:21]
	s_waitcnt vmcnt(7)
	v_mfma_f32_16x16x32_bf16 v[14:17], v[120:123], v[48:51], v[14:17]
	v_mfma_f32_16x16x32_bf16 v[10:13], v[158:161], v[48:51], v[10:13]
	s_waitcnt vmcnt(6)
	v_mfma_f32_16x16x32_bf16 v[6:9], v[120:123], v[44:47], v[6:9]
	v_mfma_f32_16x16x32_bf16 v[2:5], v[158:161], v[44:47], v[2:5]
	s_setprio 0
	s_setprio 1
	s_waitcnt vmcnt(5) lgkmcnt(3)
	v_mfma_f32_16x16x32_bf16 v[22:25], v[162:165], v[80:83], v[22:25]
	s_waitcnt lgkmcnt(1)
	v_mfma_f32_16x16x32_bf16 v[18:21], v[174:177], v[80:83], v[18:21]
	s_waitcnt vmcnt(4)
	v_mfma_f32_16x16x32_bf16 v[14:17], v[162:165], v[64:67], v[14:17]
	v_mfma_f32_16x16x32_bf16 v[10:13], v[174:177], v[64:67], v[10:13]
	s_waitcnt vmcnt(3)
	v_mfma_f32_16x16x32_bf16 v[6:9], v[162:165], v[68:71], v[6:9]
	v_mfma_f32_16x16x32_bf16 v[2:5], v[174:177], v[68:71], v[2:5]
	s_setprio 0
	s_setprio 1
	s_waitcnt vmcnt(2)
	v_mfma_f32_16x16x32_bf16 v[22:25], v[166:169], v[40:43], v[22:25]
	s_waitcnt lgkmcnt(0)
	v_mfma_f32_16x16x32_bf16 v[18:21], v[178:181], v[40:43], v[18:21]
	s_waitcnt vmcnt(1)
	v_mfma_f32_16x16x32_bf16 v[14:17], v[166:169], v[96:99], v[14:17]
	v_mfma_f32_16x16x32_bf16 v[10:13], v[178:181], v[96:99], v[10:13]
	s_waitcnt vmcnt(0)
	v_mfma_f32_16x16x32_bf16 v[6:9], v[166:169], v[88:91], v[6:9]
	v_mfma_f32_16x16x32_bf16 v[2:5], v[178:181], v[88:91], v[2:5]
	s_setprio 0
	s_barrier
	global_load_dword v26, v173, s[26:27]
	v_lshl_add_u64 v[28:29], v[126:127], 2, s[26:27]
	global_load_dword v28, v[28:29], off
	v_lshl_add_u64 v[30:31], v[128:129], 2, s[26:27]
	global_load_dword v30, v[30:31], off
	s_ashr_i32 s0, s28, 11
	v_and_b32_e32 v27, 7, v0
	v_bitop3_b32 v31, v170, v0, 7 bitop3:0x78
	s_and_b32 s1, s28, 0x7e0
	v_lshrrev_b32_e32 v48, 3, v0
	s_mulk_i32 s0, 0x180
	v_lshlrev_b32_e32 v29, 7, v124
	v_lshlrev_b32_e32 v40, 7, v126
	v_lshlrev_b32_e32 v42, 7, v128
	v_pk_add_f32 v[34:35], v[130:131], v[6:7]
	v_pk_add_f32 v[36:37], v[148:149], v[4:5]
	v_pk_add_f32 v[38:39], v[142:143], v[2:3]
	v_lshlrev_b32_e32 v2, 4, v0
	v_lshrrev_b32_e32 v6, 3, v125
	v_lshlrev_b32_e32 v3, 4, v31
	v_bitop3_b32 v4, v170, v27, 4 bitop3:0x36
	s_lshl_b32 s2, s1, 2
	v_xor_b32_e32 v5, v48, v0
	s_ashr_i32 s1, s0, 31
	v_and_b32_e32 v27, 0x70, v2
	v_xor_b32_e32 v7, v6, v0
	v_or_b32_e32 v31, v29, v3
	v_lshlrev_b32_e32 v4, 4, v4
	v_or_b32_e32 v49, v40, v3
	v_or_b32_e32 v50, v42, v3
	v_or_b32_e32 v2, s0, v48
	v_lshlrev_b32_e32 v5, 4, v5
	s_add_u32 s2, s4, s2
	v_mov_b32_e32 v3, s1
	v_pk_add_f32 v[24:25], v[136:137], v[24:25]
	v_pk_add_f32 v[22:23], v[134:135], v[22:23]
	v_pk_add_f32 v[20:21], v[150:151], v[20:21]
	v_pk_add_f32 v[18:19], v[144:145], v[18:19]
	v_lshlrev_b32_e32 v7, 4, v7
	v_or_b32_e32 v29, v29, v4
	v_or_b32_e32 v53, v40, v4
	v_or_b32_e32 v54, v42, v4
	v_and_b32_e32 v40, 0x70, v5
	s_addc_u32 s3, s5, 0
	v_lshlrev_b64 v[4:5], 13, v[2:3]
	v_or_b32_e32 v2, s0, v6
	v_pk_add_f32 v[16:17], v[138:139], v[16:17]
	v_pk_add_f32 v[14:15], v[132:133], v[14:15]
	v_pk_add_f32 v[12:13], v[152:153], v[12:13]
	v_pk_add_f32 v[10:11], v[146:147], v[10:11]
	v_pk_add_f32 v[32:33], v[140:141], v[8:9]
	v_lshl_or_b32 v52, v6, 7, v27
	v_and_b32_e32 v42, 0x70, v7
	v_lshl_add_u64 v[44:45], s[2:3], 0, v[4:5]
	v_lshlrev_b64 v[46:47], 13, v[2:3]
	v_lshl_or_b32 v51, v48, 7, v27
	v_mov_b32_e32 v41, 0
	v_mov_b32_e32 v43, v41
	s_waitcnt vmcnt(2)
	v_pk_add_f32 v[4:5], v[26:27], v[24:25] op_sel_hi:[0,1]
	v_pk_add_f32 v[2:3], v[26:27], v[22:23] op_sel_hi:[0,1]
	v_pk_add_f32 v[8:9], v[26:27], v[20:21] op_sel_hi:[0,1]
	v_pk_add_f32 v[6:7], v[26:27], v[18:19] op_sel_hi:[0,1]
	ds_write_b128 v31, v[2:5]
	ds_write_b128 v29, v[6:9]
	s_waitcnt vmcnt(1)
	v_pk_add_f32 v[4:5], v[28:29], v[16:17] op_sel_hi:[0,1]
	v_pk_add_f32 v[2:3], v[28:29], v[14:15] op_sel_hi:[0,1]
	v_pk_add_f32 v[8:9], v[28:29], v[12:13] op_sel_hi:[0,1]
	v_pk_add_f32 v[6:7], v[28:29], v[10:11] op_sel_hi:[0,1]
	s_waitcnt vmcnt(0)
	v_pk_add_f32 v[12:13], v[30:31], v[32:33] op_sel_hi:[0,1]
	v_pk_add_f32 v[10:11], v[30:31], v[34:35] op_sel_hi:[0,1]
	v_pk_add_f32 v[16:17], v[30:31], v[36:37] op_sel_hi:[0,1]
	v_pk_add_f32 v[14:15], v[30:31], v[38:39] op_sel_hi:[0,1]
	ds_write_b128 v49, v[2:5]
	ds_write_b128 v53, v[6:9]
	ds_write_b128 v50, v[10:13]
	ds_write_b128 v54, v[14:17]
	s_waitcnt lgkmcnt(0)
	s_barrier
	ds_read_b128 v[2:5], v51
	ds_read_b128 v[6:9], v52
	v_lshl_add_u64 v[10:11], v[44:45], 0, v[40:41]
	v_lshl_add_u64 v[12:13], s[2:3], 0, v[46:47]
	v_lshl_add_u64 v[12:13], v[12:13], 0, v[42:43]
	s_waitcnt lgkmcnt(1)
	global_store_dwordx4 v[10:11], v[2:5], off nt
	s_waitcnt lgkmcnt(0)
	global_store_dwordx4 v[12:13], v[6:9], off nt
	v_mov_b32_e32 v13, v41
	s_nop 0
	v_lshrrev_b32_e32 v6, 3, v1
	v_lshl_or_b32 v1, v6, 7, v27
	ds_read_b128 v[2:5], v1
	v_xor_b32_e32 v1, v6, v0
	v_mov_b32_e32 v7, v41
	v_lshlrev_b32_e32 v1, 4, v1
	v_lshl_add_u64 v[8:9], v[6:7], 0, s[0:1]
	v_and_b32_e32 v6, 0x70, v1
	v_or_b32_e32 v1, 0x600, v0
	v_lshlrev_b64 v[8:9], 13, v[8:9]
	v_lshrrev_b32_e32 v12, 3, v1
	v_lshl_add_u64 v[8:9], s[2:3], 0, v[8:9]
	v_lshl_or_b32 v1, v12, 7, v27
	v_lshl_add_u64 v[10:11], v[8:9], 0, v[6:7]
	ds_read_b128 v[6:9], v1
	s_waitcnt lgkmcnt(1)
	global_store_dwordx4 v[10:11], v[2:5], off nt
	v_xor_b32_e32 v1, v12, v0
	v_lshlrev_b32_e32 v1, 4, v1
	v_lshl_add_u64 v[2:3], v[12:13], 0, s[0:1]
	v_lshlrev_b64 v[2:3], 13, v[2:3]
	v_lshl_add_u64 v[2:3], s[2:3], 0, v[2:3]
	v_and_b32_e32 v4, 0x70, v1
	v_mov_b32_e32 v5, v41
	v_lshl_add_u64 v[2:3], v[2:3], 0, v[4:5]
	s_waitcnt lgkmcnt(0)
	global_store_dwordx4 v[2:3], v[6:9], off nt
	s_nop 1
	v_or_b32_e32 v6, 0x100, v48
	v_mov_b32_e32 v7, v41
	v_lshl_or_b32 v1, v6, 7, v27
	v_lshl_add_u64 v[6:7], v[6:7], 0, s[0:1]
	ds_read_b128 v[2:5], v1
	v_lshlrev_b64 v[6:7], 13, v[6:7]
	v_lshl_add_u64 v[6:7], s[2:3], 0, v[6:7]
	v_or_b32_e32 v1, 0xa00, v0
	v_lshl_add_u64 v[10:11], v[6:7], 0, v[40:41]
	v_lshrrev_b32_e32 v40, 3, v1
	v_lshl_or_b32 v1, v40, 7, v27
	ds_read_b128 v[6:9], v1
	s_waitcnt lgkmcnt(1)
	global_store_dwordx4 v[10:11], v[2:5], off nt
	v_xor_b32_e32 v0, v40, v0
	v_lshlrev_b32_e32 v0, 4, v0
	v_lshl_add_u64 v[2:3], v[40:41], 0, s[0:1]
	v_lshlrev_b64 v[2:3], 13, v[2:3]
	v_lshl_add_u64 v[2:3], s[2:3], 0, v[2:3]
	v_and_b32_e32 v40, 0x70, v0
	v_lshl_add_u64 v[0:1], v[2:3], 0, v[40:41]
	s_waitcnt lgkmcnt(0)
	global_store_dwordx4 v[0:1], v[6:9], off nt
	s_endpgm
